# baseline (speedup 1.0000x reference)
.LBB2_6:
	s_add_i32 s64, s64, 1
	s_add_u32 s68, s68, 0x2000
	s_addc_u32 s69, s69, 0
	s_add_u32 s74, s74, 0x2000
	s_addc_u32 s75, s75, 0
	s_add_i32 s82, s65, s64
	s_cmp_eq_u32 s82, 1
	s_cbranch_scc1 .Lattn_last_step
	v_mov_b32_e32 v120, v114
	v_mov_b32_e32 v121, v115
	s_add_i32 s37, s37, 0x4000
	s_cmp_eq_u32 s37, 0xc000
	s_cselect_b32 s37, 0, s37
	s_add_i32 s48, s40, s64
	s_add_i32 s48, s48, -1
	v_or_b32_e32 v114, s37, v57
	v_or_b32_e32 v115, s37, v81
	s_cmp_eq_u32 s55, 0
	s_cbranch_scc0 .Lattn_pre_hi
	v_mov_b32_e32 v120, v114
	v_mov_b32_e32 v121, v115
	s_branch .Lattn_pre_done
.Lattn_pre_hi:
	s_setprio 1

.Lattn_A:
	s_setprio 0
	ds_read_b128 v[34:37], v114
	ds_read_b128 v[38:41], v114 offset:2048
	ds_read_b128 v[42:45], v114 offset:4096
	ds_read_b128 v[110:113], v115 offset:2048
	ds_read_b128 v[46:49], v114 offset:6144
	s_add_i32 s48, s66, s64
	s_cmp_lg_u32 s48, 1
	s_waitcnt lgkmcnt(4)
	v_mfma_f32_16x16x32_f16 v[34:37], v[34:37], v[6:9], v[30:33]
	s_waitcnt lgkmcnt(2)
	v_mfma_f32_16x16x32_f16 v[102:105], v[42:45], v[6:9], v[30:33]
	ds_read_b128 v[42:45], v115
	v_mfma_f32_16x16x32_f16 v[38:41], v[38:41], v[6:9], v[30:33]
	s_waitcnt lgkmcnt(1)
	v_mfma_f32_16x16x32_f16 v[106:109], v[46:49], v[6:9], v[30:33]
	s_waitcnt lgkmcnt(0)
	v_mfma_f32_16x16x32_f16 v[46:49], v[42:45], v[2:5], v[34:37]
	s_nop 2
	ds_read_b128 v[34:37], v115 offset:4096
	v_mfma_f32_16x16x32_f16 v[42:45], v[110:113], v[2:5], v[38:41]
	ds_read_b128 v[110:113], v115 offset:6144
	s_waitcnt lgkmcnt(0)
	v_mfma_f32_16x16x32_f16 v[38:41], v[34:37], v[2:5], v[102:105]
	v_mfma_f32_16x16x32_f16 v[34:37], v[110:113], v[2:5], v[106:109]
	s_cbranch_scc1 .LBB2_12
	v_cndmask_b32_e64 v69, v46, v100, s[2:3]
	v_cndmask_b32_e64 v46, v69, v46, s[4:5]
	v_cndmask_b32_e64 v47, v100, v47, s[4:5]
	v_cndmask_b32_e64 v48, v48, v100, s[6:7]
	v_cndmask_b32_e64 v49, v49, v100, s[8:9]
	v_cndmask_b32_e64 v42, v42, v100, s[10:11]
	v_cndmask_b32_e64 v43, v43, v100, s[12:13]
	v_cndmask_b32_e64 v44, v44, v100, s[14:15]
	v_cndmask_b32_e64 v45, v45, v100, s[16:17]
	v_cndmask_b32_e64 v38, v38, v100, s[18:19]
	v_cndmask_b32_e64 v39, v39, v100, s[20:21]
	v_cndmask_b32_e64 v40, v40, v100, s[22:23]
	v_cndmask_b32_e64 v41, v41, v100, s[24:25]
	v_cndmask_b32_e64 v34, v34, v100, s[26:27]
	v_cndmask_b32_e64 v35, v35, v100, s[28:29]
	v_cndmask_b32_e64 v36, v36, v100, s[30:31]
	v_cndmask_b32_e64 v37, v37, v100, s[34:35]
